# v39 + retention unit: the second q/rotary load group is issued together with the first (one exposed cold-load latency less per unit)
# baseline (speedup 1.0000x reference)
.LBB0_938:
	s_and_b32 s94, s10, 7
	v_cvt_f32_ubyte0_e32 v2, s94
	v_sub_f32_e32 v2, 0xc0a00000, v2
	v_cmp_gt_f32_e32 vcc, s53, v2
	s_and_b64 s[0:1], vcc, exec
	s_cselect_b32 s0, 0xffffffc0, 0
	v_cndmask_b32_e32 v3, 0, v210, vcc
	v_add_f32_e32 v2, v2, v3
	v_exp_f32_e32 v2, v2
	v_mov_b32_e32 v141, v125
	v_mov_b32_e32 v143, v125
	v_mov_b32_e32 v27, v125
	v_ldexp_f32 v2, v2, s0
	v_sub_f32_e32 v2, 1.0, v2
	s_mov_b32 s0, 0x800000
	v_cmp_gt_f32_e32 vcc, s0, v2
	s_and_b64 s[0:1], vcc, exec
	s_cselect_b32 s0, 32, 0
	v_ldexp_f32 v2, v2, s0
	v_log_f32_e32 v2, v2
	s_and_b32 s11, s81, 0xffffff80
	v_or_b32_e32 v8, s11, v123
	v_cndmask_b32_e32 v3, 0, v211, vcc
	v_mul_lo_u32 v124, v8, s96
	v_sub_f32_e32 v215, v2, v3
	s_lshl_b32 s84, s94, 8
	v_lshl_add_u64 v[2:3], v[124:125], 1, s[82:83]
	v_lshl_add_u64 v[4:5], v[2:3], 0, s[84:85]
	v_lshl_add_u64 v[4:5], v[4:5], 0, s[90:91]
	v_lshl_add_u64 v[6:7], v[4:5], 0, v[140:141]
	v_lshl_add_u64 v[4:5], v[4:5], 0, v[142:143]
	v_lshlrev_b32_e32 v26, 6, v8
	global_load_dwordx4 v[216:219], v[6:7], off
	global_load_dwordx4 v[220:223], v[4:5], off
	v_lshlrev_b64 v[4:5], 2, v[26:27]
	v_lshl_add_u64 v[6:7], v[126:127], 0, v[4:5]
	v_lshl_add_u64 v[4:5], v[128:129], 0, v[4:5]
	global_load_dwordx4 v[98:101], v[6:7], off offset:16
	global_load_dwordx4 v[114:117], v[6:7], off
	global_load_dwordx4 v[102:105], v[4:5], off offset:16
	global_load_dwordx4 v[118:121], v[4:5], off
	s_lshl_b32 s0, s94, 9
	s_mov_b32 s1, s85
	v_add_u32_e32 v10, 0x98000, v124
	v_mov_b32_e32 v11, v125
	v_lshl_add_u64 v[2:3], v[2:3], 0, s[0:1]
	v_lshl_add_u64 v[10:11], v[10:11], 1, s[82:83]
	v_lshl_add_u64 v[2:3], v[2:3], 0, v[140:141]
	v_lshl_add_u64 v[12:13], v[10:11], 0, s[84:85]
	v_lshl_add_u64 v[6:7], v[2:3], 0, s[92:93]
	v_add_co_u32_e32 v2, vcc, s97, v2
	v_lshl_add_u64 v[12:13], v[12:13], 0, s[90:91]
	s_nop 0
	v_addc_co_u32_e32 v3, vcc, 0, v3, vcc
	v_lshl_add_u64 v[14:15], v[12:13], 0, v[140:141]
	v_lshl_add_u64 v[12:13], v[12:13], 0, v[142:143]
	global_load_dwordx4 v[2:5], v[2:3], off offset:2048
	s_nop 0
	global_load_dwordx4 v[6:9], v[6:7], off offset:256
	s_nop 0
	global_load_dwordx4 v[106:109], v[14:15], off
	global_load_dwordx4 v[110:113], v[12:13], off
	v_or_b32_e32 v12, 0x800, v26
	v_mov_b32_e32 v13, v125
	v_lshlrev_b64 v[12:13], 2, v[12:13]
	v_lshl_add_u64 v[14:15], v[126:127], 0, v[12:13]
	v_lshl_add_u64 v[12:13], v[128:129], 0, v[12:13]
	global_load_dwordx4 v[74:77], v[14:15], off offset:16
	global_load_dwordx4 v[90:93], v[14:15], off
	global_load_dwordx4 v[78:81], v[12:13], off offset:16
	global_load_dwordx4 v[94:97], v[12:13], off
	v_add_u32_e32 v18, 0x130000, v124
	v_mov_b32_e32 v19, v125
	v_lshl_add_u64 v[10:11], v[10:11], 0, s[0:1]
	v_lshl_add_u64 v[18:19], v[18:19], 1, s[82:83]
	v_lshl_add_u64 v[10:11], v[10:11], 0, v[140:141]
	v_lshl_add_u64 v[20:21], v[18:19], 0, s[84:85]
	v_lshl_add_u64 v[14:15], v[10:11], 0, s[92:93]
	v_add_co_u32_e32 v10, vcc, s97, v10
	v_lshl_add_u64 v[20:21], v[20:21], 0, s[90:91]
	s_nop 0
	v_addc_co_u32_e32 v11, vcc, 0, v11, vcc
	v_lshl_add_u64 v[22:23], v[20:21], 0, v[140:141]
	v_lshl_add_u64 v[20:21], v[20:21], 0, v[142:143]
	global_load_dwordx4 v[10:13], v[10:11], off offset:2048
	s_nop 0
	global_load_dwordx4 v[14:17], v[14:15], off offset:256
	s_nop 0
	global_load_dwordx4 v[82:85], v[22:23], off
	global_load_dwordx4 v[86:89], v[20:21], off
	v_or_b32_e32 v20, 0x1000, v26
	v_mov_b32_e32 v21, v125
	v_lshlrev_b64 v[20:21], 2, v[20:21]
	v_lshl_add_u64 v[22:23], v[126:127], 0, v[20:21]
	v_lshl_add_u64 v[20:21], v[128:129], 0, v[20:21]
	global_load_dwordx4 v[58:61], v[22:23], off offset:16
	global_load_dwordx4 v[66:69], v[22:23], off
	global_load_dwordx4 v[62:65], v[20:21], off offset:16
	global_load_dwordx4 v[70:73], v[20:21], off
	v_add_u32_e32 v124, 0x1c8000, v124
	v_lshl_add_u64 v[28:29], v[124:125], 1, s[82:83]
	v_or_b32_e32 v124, 0x1800, v26
	v_lshl_add_u64 v[18:19], v[18:19], 0, s[0:1]
	v_lshlrev_b64 v[26:27], 2, v[124:125]
	v_lshl_add_u64 v[18:19], v[18:19], 0, v[140:141]
	v_lshl_add_u64 v[30:31], v[28:29], 0, s[84:85]
	v_lshl_add_u64 v[22:23], v[18:19], 0, s[92:93]
	v_add_co_u32_e32 v18, vcc, s97, v18
	v_lshl_add_u64 v[30:31], v[30:31], 0, s[90:91]
	s_nop 0
	v_addc_co_u32_e32 v19, vcc, 0, v19, vcc
	v_lshl_add_u64 v[32:33], v[30:31], 0, v[140:141]
	global_load_dwordx4 v[18:21], v[18:19], off offset:2048
	s_nop 0
	global_load_dwordx4 v[22:25], v[22:23], off offset:256
	v_lshl_add_u64 v[30:31], v[30:31], 0, v[142:143]
	global_load_dwordx4 v[50:53], v[32:33], off
	global_load_dwordx4 v[54:57], v[30:31], off
	v_lshl_add_u64 v[30:31], v[126:127], 0, v[26:27]
	v_lshl_add_u64 v[26:27], v[128:129], 0, v[26:27]
	global_load_dwordx4 v[34:37], v[30:31], off offset:16
	global_load_dwordx4 v[42:45], v[30:31], off
	global_load_dwordx4 v[38:41], v[26:27], off offset:16
	global_load_dwordx4 v[46:49], v[26:27], off
	v_lshl_add_u64 v[26:27], v[28:29], 0, s[0:1]
	v_lshl_add_u64 v[26:27], v[26:27], 0, v[140:141]
	v_lshl_add_u64 v[28:29], v[26:27], 0, s[92:93]
	v_add_co_u32_e32 v26, vcc, s97, v26
	s_mov_b64 s[0:1], 0x4800
	s_nop 0
	v_addc_co_u32_e32 v27, vcc, 0, v27, vcc
	s_waitcnt vmcnt(29)
	v_lshlrev_b32_e32 v224, 16, v216
	s_waitcnt vmcnt(28)
	v_lshlrev_b32_e32 v225, 16, v220
	v_and_b32_e32 v227, 0xffff0000, v220
	v_and_b32_e32 v226, 0xffff0000, v216
	v_lshlrev_b32_e32 v228, 16, v217
	v_and_b32_e32 v220, 0xffff0000, v217
	v_lshlrev_b32_e32 v217, 16, v222
	v_lshlrev_b32_e32 v216, 16, v218
	v_and_b32_e32 v231, 0xffff0000, v222
	v_and_b32_e32 v230, 0xffff0000, v218
	v_lshlrev_b32_e32 v232, 16, v219
	v_and_b32_e32 v222, 0xffff0000, v219
	s_waitcnt vmcnt(26)
	v_mov_b32_e32 v218, v114
	s_waitcnt vmcnt(24)
	v_mov_b32_e32 v219, v118
	v_pk_mul_f32 v[218:219], v[218:219], v[224:225]
	v_lshlrev_b32_e32 v229, 16, v221
	v_sub_f32_e32 v114, v218, v219
	v_add_f32_e32 v118, v218, v219
	v_cndmask_b32_e64 v114, v118, v114, s[6:7]
	v_mov_b32_e32 v118, v115
	v_mul_f32_e32 v124, 0x3db504f3, v114
	v_pk_mul_f32 v[114:115], v[118:119], v[226:227]
	v_and_b32_e32 v221, 0xffff0000, v221
	v_sub_f32_e32 v118, v114, v115
	v_add_f32_e32 v114, v114, v115
	v_cndmask_b32_e64 v114, v114, v118, s[6:7]
	v_mul_f32_e32 v118, 0x3db504f3, v114
	v_mov_b32_e32 v114, v116
	v_mov_b32_e32 v115, v120
	v_pk_mul_f32 v[114:115], v[114:115], v[228:229]
	v_mov_b32_e32 v120, v117
	v_sub_f32_e32 v116, v114, v115
	v_add_f32_e32 v114, v114, v115
	v_cndmask_b32_e64 v114, v114, v116, s[6:7]
	v_mul_f32_e32 v116, 0x3db504f3, v114
	v_pk_mul_f32 v[114:115], v[120:121], v[220:221]
	v_lshlrev_b32_e32 v233, 16, v223
	v_sub_f32_e32 v117, v114, v115
	v_add_f32_e32 v114, v114, v115
	v_cndmask_b32_e64 v114, v114, v117, s[6:7]
	v_mul_f32_e32 v117, 0x3db504f3, v114
	v_mov_b32_e32 v114, v98
	v_mov_b32_e32 v115, v102
	v_pk_mul_f32 v[114:115], v[114:115], v[216:217]
	v_and_b32_e32 v223, 0xffff0000, v223
	v_sub_f32_e32 v98, v114, v115
	v_add_f32_e32 v102, v114, v115
	v_cndmask_b32_e64 v98, v102, v98, s[6:7]
	v_mov_b32_e32 v102, v99
	v_mul_f32_e32 v114, 0x3db504f3, v98
	v_pk_mul_f32 v[98:99], v[102:103], v[230:231]
	global_load_dwordx4 v[30:33], v[26:27], off offset:2048
	s_nop 0
	global_load_dwordx4 v[26:29], v[28:29], off offset:256
	v_sub_f32_e32 v102, v98, v99
	v_add_f32_e32 v98, v98, v99
	v_cndmask_b32_e64 v98, v98, v102, s[6:7]
	v_mul_f32_e32 v102, 0x3db504f3, v98
	v_mov_b32_e32 v98, v100
	v_mov_b32_e32 v99, v104
	v_pk_mul_f32 v[98:99], v[98:99], v[232:233]
	v_mov_b32_e32 v104, v101
	v_sub_f32_e32 v100, v98, v99
	v_add_f32_e32 v98, v98, v99
	v_cndmask_b32_e64 v98, v98, v100, s[6:7]
	v_mul_f32_e32 v103, 0x3db504f3, v98
	v_pk_mul_f32 v[98:99], v[104:105], v[222:223]
	s_waitcnt vmcnt(22)
	v_and_b32_e32 v105, 0xffff0000, v111
	v_sub_f32_e32 v100, v98, v99
	v_add_f32_e32 v98, v98, v99
	v_cndmask_b32_e64 v98, v98, v100, s[6:7]
	v_mul_f32_e32 v101, 0x3db504f3, v98
	v_cvt_pk_bf16_f32 v98, v124, v118
	v_cvt_pk_bf16_f32 v99, v116, v117
	v_cvt_pk_bf16_f32 v100, v114, v102
	v_cvt_pk_bf16_f32 v101, v103, v101
	ds_write_b128 v198, v[98:101]
	v_lshlrev_b32_e32 v99, 16, v110
	v_lshlrev_b32_e32 v98, 16, v106
	v_and_b32_e32 v101, 0xffff0000, v110
	v_and_b32_e32 v100, 0xffff0000, v106
	v_lshlrev_b32_e32 v103, 16, v111
	v_lshlrev_b32_e32 v102, 16, v107
	v_and_b32_e32 v104, 0xffff0000, v107
	v_lshlrev_b32_e32 v107, 16, v112
	v_lshlrev_b32_e32 v106, 16, v108
	v_and_b32_e32 v111, 0xffff0000, v112
	v_and_b32_e32 v110, 0xffff0000, v108
	v_lshlrev_b32_e32 v114, 16, v109
	v_and_b32_e32 v112, 0xffff0000, v109
	s_waitcnt vmcnt(20)
	v_mov_b32_e32 v108, v90
	s_waitcnt vmcnt(18)
	v_mov_b32_e32 v109, v94
	v_pk_mul_f32 v[98:99], v[108:109], v[98:99]
	v_lshlrev_b32_e32 v115, 16, v113
	v_sub_f32_e32 v90, v98, v99
	v_add_f32_e32 v94, v98, v99
	v_cndmask_b32_e64 v90, v94, v90, s[6:7]
	v_mov_b32_e32 v94, v91
	v_mul_f32_e32 v98, 0x3db504f3, v90
	v_pk_mul_f32 v[90:91], v[94:95], v[100:101]
	v_and_b32_e32 v113, 0xffff0000, v113
	v_sub_f32_e32 v94, v90, v91
	v_add_f32_e32 v90, v90, v91
	v_cndmask_b32_e64 v90, v90, v94, s[6:7]
	v_mul_f32_e32 v94, 0x3db504f3, v90
	v_mov_b32_e32 v90, v92
	v_mov_b32_e32 v91, v96
	v_pk_mul_f32 v[90:91], v[90:91], v[102:103]
	v_mov_b32_e32 v96, v93
	v_sub_f32_e32 v92, v90, v91
	v_add_f32_e32 v90, v90, v91
	v_cndmask_b32_e64 v90, v90, v92, s[6:7]
	v_mul_f32_e32 v92, 0x3db504f3, v90
	v_pk_mul_f32 v[90:91], v[96:97], v[104:105]
	s_waitcnt vmcnt(6)
	v_lshlrev_b32_e32 v95, 16, v57
	v_sub_f32_e32 v93, v90, v91
	v_add_f32_e32 v90, v90, v91
	v_cndmask_b32_e64 v90, v90, v93, s[6:7]
	v_mul_f32_e32 v93, 0x3db504f3, v90
	v_mov_b32_e32 v90, v74
	v_mov_b32_e32 v91, v78
	v_pk_mul_f32 v[90:91], v[90:91], v[106:107]
	v_and_b32_e32 v57, 0xffff0000, v57
	v_sub_f32_e32 v74, v90, v91
	v_add_f32_e32 v78, v90, v91
	v_cndmask_b32_e64 v74, v78, v74, s[6:7]
	v_mov_b32_e32 v78, v75
	v_mul_f32_e32 v90, 0x3db504f3, v74
	v_pk_mul_f32 v[74:75], v[78:79], v[110:111]
	v_lshlrev_b32_e32 v91, 16, v89
	v_sub_f32_e32 v78, v74, v75
	v_add_f32_e32 v74, v74, v75
	v_cndmask_b32_e64 v74, v74, v78, s[6:7]
	v_mul_f32_e32 v78, 0x3db504f3, v74
	v_mov_b32_e32 v74, v76
	v_mov_b32_e32 v75, v80
	v_pk_mul_f32 v[74:75], v[74:75], v[114:115]
	v_mov_b32_e32 v80, v77
	v_sub_f32_e32 v76, v74, v75
	v_add_f32_e32 v74, v74, v75
	v_cndmask_b32_e64 v74, v74, v76, s[6:7]
	v_mul_f32_e32 v79, 0x3db504f3, v74
	v_pk_mul_f32 v[74:75], v[80:81], v[112:113]
	v_and_b32_e32 v81, 0xffff0000, v87
	v_sub_f32_e32 v76, v74, v75
	v_add_f32_e32 v74, v74, v75
	v_cndmask_b32_e64 v74, v74, v76, s[6:7]
	v_mul_f32_e32 v77, 0x3db504f3, v74
	v_cvt_pk_bf16_f32 v74, v98, v94
	v_cvt_pk_bf16_f32 v75, v92, v93
	v_cvt_pk_bf16_f32 v76, v90, v78
	v_cvt_pk_bf16_f32 v77, v79, v77
	ds_write_b128 v198, v[74:77] offset:8704
	v_lshlrev_b32_e32 v75, 16, v86
	v_lshlrev_b32_e32 v74, 16, v82
	v_and_b32_e32 v77, 0xffff0000, v86
	v_and_b32_e32 v76, 0xffff0000, v82
	v_lshlrev_b32_e32 v79, 16, v87
	v_lshlrev_b32_e32 v78, 16, v83
	v_and_b32_e32 v80, 0xffff0000, v83
	v_lshlrev_b32_e32 v83, 16, v88
	v_lshlrev_b32_e32 v82, 16, v84
	v_and_b32_e32 v87, 0xffff0000, v88
	v_and_b32_e32 v86, 0xffff0000, v84
	v_lshlrev_b32_e32 v90, 16, v85
	v_and_b32_e32 v88, 0xffff0000, v85
	v_mov_b32_e32 v84, v66
	v_mov_b32_e32 v85, v70
	v_pk_mul_f32 v[74:75], v[84:85], v[74:75]
	v_and_b32_e32 v89, 0xffff0000, v89
	v_sub_f32_e32 v66, v74, v75
	v_add_f32_e32 v70, v74, v75
	v_cndmask_b32_e64 v66, v70, v66, s[6:7]
	v_mov_b32_e32 v70, v67
	v_mul_f32_e32 v74, 0x3db504f3, v66
	v_pk_mul_f32 v[66:67], v[70:71], v[76:77]
	v_and_b32_e32 v92, 0xffff0000, v52
	v_sub_f32_e32 v70, v66, v67
	v_add_f32_e32 v66, v66, v67
	v_cndmask_b32_e64 v66, v66, v70, s[6:7]
	v_mul_f32_e32 v70, 0x3db504f3, v66
	v_mov_b32_e32 v66, v68
	v_mov_b32_e32 v67, v72
	v_pk_mul_f32 v[66:67], v[66:67], v[78:79]
	v_mov_b32_e32 v72, v69
	v_sub_f32_e32 v68, v66, v67
	v_add_f32_e32 v66, v66, v67
	v_cndmask_b32_e64 v66, v66, v68, s[6:7]
	v_mul_f32_e32 v68, 0x3db504f3, v66
	v_pk_mul_f32 v[66:67], v[72:73], v[80:81]
	v_and_b32_e32 v93, 0xffff0000, v56
	v_sub_f32_e32 v69, v66, v67
	v_add_f32_e32 v66, v66, v67
	v_cndmask_b32_e64 v66, v66, v69, s[6:7]
	v_mul_f32_e32 v69, 0x3db504f3, v66
	v_mov_b32_e32 v66, v58
	v_mov_b32_e32 v67, v62
	v_pk_mul_f32 v[66:67], v[66:67], v[82:83]
	v_lshlrev_b32_e32 v94, 16, v53
	v_sub_f32_e32 v58, v66, v67
	v_add_f32_e32 v62, v66, v67
	v_cndmask_b32_e64 v58, v62, v58, s[6:7]
	v_mov_b32_e32 v62, v59
	v_mul_f32_e32 v66, 0x3db504f3, v58
	v_pk_mul_f32 v[58:59], v[62:63], v[86:87]
	v_lshlrev_b32_e32 v86, 16, v50
	v_sub_f32_e32 v62, v58, v59
	v_add_f32_e32 v58, v58, v59
	v_cndmask_b32_e64 v58, v58, v62, s[6:7]
	v_mul_f32_e32 v62, 0x3db504f3, v58
	v_mov_b32_e32 v58, v60
	v_mov_b32_e32 v59, v64
	v_pk_mul_f32 v[58:59], v[58:59], v[90:91]
	v_mov_b32_e32 v64, v61
	v_sub_f32_e32 v60, v58, v59
	v_add_f32_e32 v58, v58, v59
	v_cndmask_b32_e64 v58, v58, v60, s[6:7]
	v_mul_f32_e32 v63, 0x3db504f3, v58
	v_pk_mul_f32 v[58:59], v[64:65], v[88:89]
	v_and_b32_e32 v88, 0xffff0000, v50
	v_sub_f32_e32 v60, v58, v59
	v_add_f32_e32 v58, v58, v59
	v_cndmask_b32_e64 v58, v58, v60, s[6:7]
	v_lshlrev_b32_e32 v50, 16, v52
	v_add_u32_e32 v52, s11, v144
	v_mul_f32_e32 v61, 0x3db504f3, v58
	v_cvt_pk_bf16_f32 v58, v74, v70
	v_cvt_pk_bf16_f32 v59, v68, v69
	v_mul_lo_u32 v124, v52, s96
	v_cvt_pk_bf16_f32 v60, v66, v62
	v_cvt_pk_bf16_f32 v61, v63, v61
	ds_write_b128 v198, v[58:61] offset:17408
	v_lshl_add_u64 v[58:59], v[124:125], 1, s[82:83]
	v_lshl_add_u64 v[58:59], v[58:59], 0, s[84:85]
	v_lshlrev_b32_e32 v124, 1, v130
	v_lshl_add_u64 v[58:59], v[58:59], 0, v[124:125]
	v_lshl_add_u64 v[96:97], v[58:59], 0, s[0:1]
	s_movk_i32 s0, 0x4000
	v_lshlrev_b32_e32 v124, 6, v52
	v_add_co_u32_e32 v58, vcc, s0, v58
	v_lshlrev_b64 v[70:71], 2, v[124:125]
	s_nop 0
	v_addc_co_u32_e32 v59, vcc, 0, v59, vcc
	v_lshl_add_u64 v[98:99], v[132:133], 0, v[70:71]
	global_load_dwordx4 v[62:65], v[58:59], off offset:2048
	s_nop 0
	global_load_dwordx4 v[58:61], v[96:97], off offset:64
	global_load_dwordx4 v[66:69], v[96:97], off offset:128
	v_lshl_add_u64 v[100:101], v[134:135], 0, v[70:71]
	global_load_dwordx4 v[70:73], v[98:99], off offset:16
	global_load_dwordx4 v[78:81], v[98:99], off
	global_load_dwordx4 v[74:77], v[100:101], off offset:16
	global_load_dwordx4 v[82:85], v[100:101], off
	global_load_dwordx4 v[224:227], v[96:97], off offset:192
	global_load_dwordx4 v[228:231], v[98:99], off offset:144
	global_load_dwordx4 v[246:249], v[98:99], off offset:128
	global_load_dwordx4 v[220:223], v[100:101], off offset:144
	global_load_dwordx2 v[232:233], v[100:101], off offset:128
	global_load_dwordx2 v[250:251], v[100:101], off offset:136
	v_lshlrev_b32_e32 v87, 16, v54
	v_and_b32_e32 v89, 0xffff0000, v54
	v_lshlrev_b32_e32 v90, 16, v51
	v_and_b32_e32 v54, 0xffff0000, v51
	v_lshlrev_b32_e32 v51, 16, v56
	v_and_b32_e32 v56, 0xffff0000, v53
	s_waitcnt vmcnt(17)
	v_mov_b32_e32 v52, v42
	s_waitcnt vmcnt(15)
	v_mov_b32_e32 v53, v46
	v_pk_mul_f32 v[52:53], v[52:53], v[86:87]
	v_lshlrev_b32_e32 v91, 16, v55
	v_sub_f32_e32 v42, v52, v53
	v_add_f32_e32 v46, v52, v53
	v_cndmask_b32_e64 v42, v46, v42, s[6:7]
	v_mov_b32_e32 v46, v43
	v_mul_f32_e32 v52, 0x3db504f3, v42
	v_pk_mul_f32 v[42:43], v[46:47], v[88:89]
	v_and_b32_e32 v55, 0xffff0000, v55
	v_sub_f32_e32 v46, v42, v43
	v_add_f32_e32 v42, v42, v43
	v_cndmask_b32_e64 v42, v42, v46, s[6:7]
	v_mul_f32_e32 v46, 0x3db504f3, v42
	v_mov_b32_e32 v42, v44
	v_mov_b32_e32 v43, v48
	v_pk_mul_f32 v[42:43], v[42:43], v[90:91]
	v_mov_b32_e32 v48, v45
	v_sub_f32_e32 v44, v42, v43
	v_add_f32_e32 v42, v42, v43
	v_cndmask_b32_e64 v42, v42, v44, s[6:7]
	v_mul_f32_e32 v44, 0x3db504f3, v42
	v_pk_mul_f32 v[42:43], v[48:49], v[54:55]
	s_movk_i32 s0, 0x1000
	v_sub_f32_e32 v45, v42, v43
	v_add_f32_e32 v42, v42, v43
	v_cndmask_b32_e64 v42, v42, v45, s[6:7]
	v_mul_f32_e32 v45, 0x3db504f3, v42
	v_mov_b32_e32 v42, v34
	v_mov_b32_e32 v43, v38
	v_pk_mul_f32 v[42:43], v[42:43], v[50:51]
	s_nop 0
	v_sub_f32_e32 v34, v42, v43
	v_add_f32_e32 v38, v42, v43
	v_cndmask_b32_e64 v34, v38, v34, s[6:7]
	v_mov_b32_e32 v38, v35
	v_mul_f32_e32 v42, 0x3db504f3, v34
	v_pk_mul_f32 v[34:35], v[38:39], v[92:93]
	s_nop 0
	v_sub_f32_e32 v38, v34, v35
	v_add_f32_e32 v34, v34, v35
	v_cndmask_b32_e64 v34, v34, v38, s[6:7]
	v_mul_f32_e32 v38, 0x3db504f3, v34
	v_mov_b32_e32 v34, v36
	v_mov_b32_e32 v35, v40
	v_pk_mul_f32 v[34:35], v[34:35], v[94:95]
	v_mov_b32_e32 v40, v37
	v_sub_f32_e32 v36, v34, v35
	v_add_f32_e32 v34, v34, v35
	v_cndmask_b32_e64 v34, v34, v36, s[6:7]
	v_mul_f32_e32 v39, 0x3db504f3, v34
	v_pk_mul_f32 v[34:35], v[40:41], v[56:57]
	s_nop 0
	v_sub_f32_e32 v36, v34, v35
	v_add_f32_e32 v34, v34, v35
	v_cndmask_b32_e64 v34, v34, v36, s[6:7]
	v_mul_f32_e32 v37, 0x3db504f3, v34
	v_cvt_pk_bf16_f32 v34, v52, v46
	v_cvt_pk_bf16_f32 v35, v44, v45
	v_cvt_pk_bf16_f32 v36, v42, v38
	v_cvt_pk_bf16_f32 v37, v39, v37
	ds_write_b128 v198, v[34:37] offset:26112
	ds_write_b128 v199, v[2:5] offset:34816
	ds_write_b128 v199, v[6:9] offset:35072
	ds_write_b128 v199, v[10:13] offset:51712
	ds_write_b128 v199, v[14:17] offset:51968
	ds_write_b128 v200, v[18:21] offset:34816
	ds_write_b128 v200, v[22:25] offset:35072
	s_waitcnt vmcnt(14)
	ds_write_b128 v200, v[30:33] offset:51712
	v_mul_f32_e32 v2, v215, v145
	v_cmp_gt_f32_e32 vcc, s53, v2
	s_waitcnt vmcnt(13)
	ds_write_b128 v200, v[26:29] offset:51968
	s_waitcnt vmcnt(12)
	v_lshlrev_b32_e32 v22, 16, v63
	v_cndmask_b32_e32 v2, 0, v210, vcc
	v_fmac_f32_e32 v2, v215, v145
	v_exp_f32_e32 v6, v2
	v_cndmask_b32_e32 v7, 0, v212, vcc
	s_waitcnt vmcnt(8)
	v_mov_b32_e32 v8, v78
	s_waitcnt vmcnt(6)
	v_mov_b32_e32 v9, v82
	v_ldexp_f32 v30, v6, v7
	v_lshlrev_b32_e32 v6, 16, v62
	v_lshlrev_b32_e32 v7, 16, v66
	v_pk_mul_f32 v[8:9], v[8:9], v[6:7]
	v_lshlrev_b32_e32 v23, 16, v67
	v_sub_f32_e32 v26, v8, v9
	v_mov_b32_e32 v8, v82
	v_mov_b32_e32 v9, v78
	v_pk_mul_f32 v[6:7], v[8:9], v[6:7]
	v_mov_b32_e32 v82, v79
	v_add_f32_e32 v38, v7, v6
	v_and_b32_e32 v7, 0xffff0000, v66
	v_and_b32_e32 v6, 0xffff0000, v62
	v_mov_b32_e32 v78, v83
	v_pk_mul_f32 v[8:9], v[82:83], v[6:7]
	v_pk_mul_f32 v[6:7], v[78:79], v[6:7]
	v_add_f32_e32 v39, v7, v6
	v_mov_b32_e32 v6, v80
	v_mov_b32_e32 v7, v84
	v_pk_mul_f32 v[6:7], v[6:7], v[22:23]
	v_sub_f32_e32 v27, v8, v9
	v_sub_f32_e32 v28, v6, v7
	v_mov_b32_e32 v24, v84
	v_mov_b32_e32 v25, v80
	v_pk_mul_f32 v[22:23], v[24:25], v[22:23]
	v_mov_b32_e32 v84, v81
	v_add_f32_e32 v40, v23, v22
	v_and_b32_e32 v23, 0xffff0000, v67
	v_and_b32_e32 v22, 0xffff0000, v63
	v_mov_b32_e32 v80, v85
	v_pk_mul_f32 v[24:25], v[84:85], v[22:23]
	v_pk_mul_f32 v[22:23], v[80:81], v[22:23]
	v_sub_f32_e32 v29, v24, v25
	v_add_f32_e32 v41, v23, v22
	v_lshlrev_b32_e32 v22, 16, v64
	v_lshlrev_b32_e32 v23, 16, v68
	v_mov_b32_e32 v24, v70
	v_mov_b32_e32 v25, v74
	v_pk_mul_f32 v[24:25], v[24:25], v[22:23]
	s_nop 0
	v_sub_f32_e32 v31, v24, v25
	v_mov_b32_e32 v24, v74
	v_mov_b32_e32 v25, v70
	v_pk_mul_f32 v[22:23], v[24:25], v[22:23]
	v_mov_b32_e32 v74, v71
	v_add_f32_e32 v46, v23, v22
	v_and_b32_e32 v23, 0xffff0000, v68
	v_and_b32_e32 v22, 0xffff0000, v64
	v_mov_b32_e32 v70, v75
	v_pk_mul_f32 v[24:25], v[74:75], v[22:23]
	v_pk_mul_f32 v[22:23], v[70:71], v[22:23]
	v_sub_f32_e32 v32, v24, v25
	v_add_f32_e32 v47, v23, v22
	v_lshlrev_b32_e32 v22, 16, v65
	v_lshlrev_b32_e32 v23, 16, v69
	v_mov_b32_e32 v24, v72
	v_mov_b32_e32 v25, v76
	v_pk_mul_f32 v[24:25], v[24:25], v[22:23]
	s_nop 0
	v_sub_f32_e32 v33, v24, v25
	v_mov_b32_e32 v24, v76
	v_mov_b32_e32 v25, v72
	v_pk_mul_f32 v[22:23], v[24:25], v[22:23]
	v_mov_b32_e32 v76, v73
	v_add_f32_e32 v48, v23, v22
	v_and_b32_e32 v23, 0xffff0000, v69
	v_and_b32_e32 v22, 0xffff0000, v65
	v_mov_b32_e32 v72, v77
	v_pk_mul_f32 v[24:25], v[76:77], v[22:23]
	v_pk_mul_f32 v[22:23], v[72:73], v[22:23]
	v_sub_f32_e32 v34, v24, v25
	v_add_f32_e32 v49, v23, v22
	v_cvt_pk_bf16_f32 v22, v26, v27
	v_mul_f32_e32 v26, v30, v26
	v_mul_f32_e32 v27, v30, v27
	v_cvt_pk_bf16_f32 v23, v28, v29
	v_cvt_pk_bf16_f32 v26, v26, v27
	v_mul_f32_e32 v27, v30, v28
	v_mul_f32_e32 v28, v30, v29
	v_cvt_pk_bf16_f32 v27, v27, v28
	v_mul_f32_e32 v28, v30, v31
	v_mul_f32_e32 v29, v30, v32
	v_cvt_pk_bf16_f32 v28, v28, v29
	v_mul_f32_e32 v29, v30, v33
	v_cvt_pk_bf16_f32 v24, v31, v32
	v_mul_f32_e32 v31, v30, v34
	v_cvt_pk_bf16_f32 v29, v29, v31
	ds_write_b128 v146, v[26:29]
	v_mul_f32_e32 v26, v30, v38
	v_mul_f32_e32 v27, v30, v39
	v_cvt_pk_bf16_f32 v26, v26, v27
	v_mul_f32_e32 v27, v30, v40
	v_mul_f32_e32 v28, v30, v41
	v_cvt_pk_bf16_f32 v27, v27, v28
	v_mul_f32_e32 v28, v30, v46
	v_mul_f32_e32 v29, v30, v47
	v_cvt_pk_bf16_f32 v28, v28, v29
	v_mul_f32_e32 v29, v30, v48
	v_mul_f32_e32 v31, v30, v49
	v_cvt_pk_bf16_f32 v29, v29, v31
	ds_write_b128 v146, v[26:29] offset:128
	s_waitcnt vmcnt(5)
	v_mov_b32_e32 v2, v224
	v_mov_b32_e32 v3, v225
	v_mov_b32_e32 v4, v226
	v_mov_b32_e32 v5, v227
	v_lshlrev_b32_e32 v27, 16, v2
	v_lshlrev_b32_e32 v26, 16, v58
	s_waitcnt vmcnt(3)
	v_mov_b32_e32 v6, v228
	v_mov_b32_e32 v7, v229
	v_mov_b32_e32 v8, v230
	v_mov_b32_e32 v9, v231
	v_mov_b32_e32 v10, v246
	v_mov_b32_e32 v11, v247
	v_mov_b32_e32 v12, v248
	v_mov_b32_e32 v13, v249
	v_mov_b32_e32 v28, v10
	s_waitcnt vmcnt(0)
	v_mov_b32_e32 v14, v220
	v_mov_b32_e32 v15, v221
	v_mov_b32_e32 v16, v222
	v_mov_b32_e32 v17, v223
	v_mov_b32_e32 v18, v232
	v_mov_b32_e32 v19, v233
	v_mov_b32_e32 v20, v250
	v_mov_b32_e32 v21, v251
	v_mov_b32_e32 v29, v18
	v_pk_mul_f32 v[28:29], v[28:29], v[26:27]
	v_cvt_pk_bf16_f32 v25, v33, v34
	v_cvt_pk_bf16_f32 v38, v38, v39
	v_cvt_pk_bf16_f32 v39, v40, v41
	v_cvt_pk_bf16_f32 v40, v46, v47
	v_cvt_pk_bf16_f32 v41, v48, v49
	s_nop 0
	v_sub_f32_e32 v54, v28, v29
	v_mov_b32_e32 v28, v18
	v_mov_b32_e32 v29, v10
	v_pk_mul_f32 v[26:27], v[28:29], v[26:27]
	v_mov_b32_e32 v10, v19
	v_add_f32_e32 v62, v27, v26
	v_and_b32_e32 v27, 0xffff0000, v2
	v_and_b32_e32 v26, 0xffff0000, v58
	v_mov_b32_e32 v18, v11
	v_pk_mul_f32 v[10:11], v[10:11], v[26:27]
	v_pk_mul_f32 v[28:29], v[18:19], v[26:27]
	v_add_f32_e32 v63, v11, v10
	v_lshlrev_b32_e32 v11, 16, v3
	v_lshlrev_b32_e32 v10, 16, v59
	v_mov_b32_e32 v18, v12
	v_mov_b32_e32 v19, v20
	v_pk_mul_f32 v[18:19], v[18:19], v[10:11]
	v_and_b32_e32 v3, 0xffff0000, v3
	v_sub_f32_e32 v56, v18, v19
	v_mov_b32_e32 v18, v20
	v_mov_b32_e32 v19, v12
	v_pk_mul_f32 v[10:11], v[18:19], v[10:11]
	v_and_b32_e32 v2, 0xffff0000, v59
	v_mov_b32_e32 v20, v13
	v_mov_b32_e32 v12, v21
	v_add_f32_e32 v64, v11, v10
	v_pk_mul_f32 v[10:11], v[20:21], v[2:3]
	v_pk_mul_f32 v[2:3], v[12:13], v[2:3]
	v_sub_f32_e32 v57, v10, v11
	v_add_f32_e32 v65, v3, v2
	v_lshlrev_b32_e32 v3, 16, v4
	v_lshlrev_b32_e32 v2, 16, v60
	v_mov_b32_e32 v10, v6
	v_mov_b32_e32 v11, v14
	v_pk_mul_f32 v[10:11], v[10:11], v[2:3]
	v_sub_f32_e32 v55, v28, v29
	v_sub_f32_e32 v66, v10, v11
	v_mov_b32_e32 v10, v14
	v_mov_b32_e32 v11, v6
	v_pk_mul_f32 v[2:3], v[10:11], v[2:3]
	v_mov_b32_e32 v14, v7
	v_add_f32_e32 v67, v3, v2
	v_and_b32_e32 v3, 0xffff0000, v4
	v_and_b32_e32 v2, 0xffff0000, v60
	v_mov_b32_e32 v6, v15
	v_pk_mul_f32 v[10:11], v[14:15], v[2:3]
	v_pk_mul_f32 v[2:3], v[6:7], v[2:3]
	v_mov_b32_e32 v6, v8
	v_add_f32_e32 v69, v3, v2
	v_lshlrev_b32_e32 v3, 16, v5
	v_lshlrev_b32_e32 v2, 16, v61
	v_mov_b32_e32 v7, v16
	v_pk_mul_f32 v[6:7], v[6:7], v[2:3]
	v_sub_f32_e32 v68, v10, v11
	v_sub_f32_e32 v70, v6, v7
	v_mov_b32_e32 v6, v16
	v_mov_b32_e32 v7, v8
	v_pk_mul_f32 v[2:3], v[6:7], v[2:3]
	v_mov_b32_e32 v16, v9
	v_add_f32_e32 v71, v3, v2
	v_and_b32_e32 v3, 0xffff0000, v5
	v_and_b32_e32 v2, 0xffff0000, v61
	v_mov_b32_e32 v8, v17
	v_pk_mul_f32 v[4:5], v[16:17], v[2:3]
	v_pk_mul_f32 v[2:3], v[8:9], v[2:3]
	v_sub_f32_e32 v72, v4, v5
	v_add_f32_e32 v73, v3, v2
	v_mul_f32_e32 v2, v30, v54
	v_mul_f32_e32 v3, v30, v55
	v_cvt_pk_bf16_f32 v2, v2, v3
	v_mul_f32_e32 v3, v30, v56
	v_mul_f32_e32 v4, v30, v57
	v_cvt_pk_bf16_f32 v3, v3, v4
	v_mul_f32_e32 v4, v30, v66
	v_mul_f32_e32 v5, v30, v68
	v_cvt_pk_bf16_f32 v4, v4, v5
	v_mul_f32_e32 v5, v30, v70
	v_mul_f32_e32 v6, v30, v72
	v_cvt_pk_bf16_f32 v5, v5, v6
	ds_write_b128 v146, v[2:5] offset:64
	v_mul_f32_e32 v2, v30, v62
	v_mul_f32_e32 v3, v30, v63
	v_cvt_pk_bf16_f32 v2, v2, v3
	v_mul_f32_e32 v3, v30, v64
	v_mul_f32_e32 v4, v30, v65
	v_cvt_pk_bf16_f32 v3, v3, v4
	v_mul_f32_e32 v4, v30, v67
	v_mul_f32_e32 v5, v30, v69
	v_cvt_pk_bf16_f32 v4, v4, v5
	v_mul_f32_e32 v5, v30, v71
	v_mul_f32_e32 v6, v30, v73
	v_cvt_pk_bf16_f32 v5, v5, v6
	v_add_co_u32_e32 v6, vcc, s0, v138
	ds_write_b128 v146, v[2:5] offset:192
	s_nop 0
	v_addc_co_u32_e32 v7, vcc, 0, v139, vcc
	global_load_dwordx4 v[30:33], v[138:139], off
	global_load_dwordx4 v[18:21], v[138:139], off offset:64
	global_load_dwordx4 v[10:13], v[138:139], off offset:128
	global_load_dwordx4 v[2:5], v[138:139], off offset:192
	global_load_dwordx4 v[34:37], v[6:7], off
	global_load_dwordx4 v[26:29], v[6:7], off offset:64
	global_load_dwordx4 v[14:17], v[6:7], off offset:128
	s_nop 0
	global_load_dwordx4 v[6:9], v[6:7], off offset:192
	s_waitcnt lgkmcnt(0)
	s_barrier
	ds_read_b128 v[42:45], v201
	ds_read_b128 v[50:53], v201 offset:64
	v_cvt_pk_bf16_f32 v46, v54, v55
	v_cvt_pk_bf16_f32 v47, v56, v57
	ds_read_b128 v[54:57], v201 offset:128
	s_waitcnt lgkmcnt(2)
	v_mfma_f32_16x16x32_bf16 v[58:61], v[42:45], v[22:25], 0
	v_cvt_pk_bf16_f32 v48, v66, v68
	v_cvt_pk_bf16_f32 v49, v70, v72
	v_mul_f32_e32 v45, v215, v147
	s_waitcnt lgkmcnt(1)
	v_mfma_f32_16x16x32_bf16 v[50:53], v[50:53], v[46:49], v[58:61]
	v_cmp_gt_f32_e32 vcc, s53, v45
	v_cvt_pk_bf16_f32 v42, v62, v63
	v_cvt_pk_bf16_f32 v43, v64, v65
	v_cvt_pk_bf16_f32 v44, v67, v69
	v_readlane_b32 s0, v254, 16
	s_nop 2
	ds_read_b128 v[58:61], v201 offset:192
	v_cndmask_b32_e32 v45, 0, v210, vcc
	v_fmac_f32_e32 v45, v215, v147
	s_waitcnt lgkmcnt(1)
	v_mfma_f32_16x16x32_bf16 v[50:53], v[54:57], v[38:41], v[50:53]
	v_exp_f32_e32 v54, v45
	v_cndmask_b32_e32 v55, 0, v212, vcc
	v_cvt_pk_bf16_f32 v45, v71, v73
	v_readlane_b32 s1, v254, 17
	v_ldexp_f32 v54, v54, v55
	v_mul_f32_e32 v55, v215, v148
	v_cmp_gt_f32_e32 vcc, s53, v55
	s_waitcnt lgkmcnt(0)
	v_mfma_f32_16x16x32_bf16 v[50:53], v[58:61], v[42:45], v[50:53]
	ds_read_b128 v[58:61], v201 offset:4416
	v_cndmask_b32_e32 v55, 0, v210, vcc
	v_fmac_f32_e32 v55, v215, v148
	v_exp_f32_e32 v55, v55
	ds_read_b128 v[62:65], v201 offset:4480
	s_nop 2
	v_mul_f32_e32 v50, v54, v50
	v_cndmask_b32_e64 v66, 0, v50, s[0:1]
	v_cndmask_b32_e32 v50, 0, v212, vcc
	v_ldexp_f32 v50, v55, v50
	v_mul_f32_e32 v50, v50, v51
	v_mul_f32_e32 v51, v215, v149
	ds_read_b128 v[54:57], v201 offset:4352
	v_cmp_gt_f32_e32 vcc, s53, v51
	v_readlane_b32 s0, v254, 18
	v_readlane_b32 s1, v254, 19
	v_cndmask_b32_e32 v51, 0, v210, vcc
	v_fmac_f32_e32 v51, v215, v149
	v_exp_f32_e32 v51, v51
	v_cndmask_b32_e64 v67, 0, v50, s[0:1]
	v_cndmask_b32_e32 v50, 0, v212, vcc
	s_waitcnt lgkmcnt(0)
	v_mfma_f32_16x16x32_bf16 v[54:57], v[54:57], v[22:25], 0
	v_ldexp_f32 v50, v51, v50
	v_mul_f32_e32 v51, v215, v150
	v_cmp_gt_f32_e32 vcc, s53, v51
	v_mfma_f32_16x16x32_bf16 v[54:57], v[58:61], v[46:49], v[54:57]
	v_mul_f32_e32 v50, v50, v52
	v_cndmask_b32_e32 v51, 0, v210, vcc
	v_fmac_f32_e32 v51, v215, v150
	v_exp_f32_e32 v51, v51
	v_cndmask_b32_e64 v68, 0, v50, s[12:13]
	v_cndmask_b32_e32 v50, 0, v212, vcc
	ds_read_b128 v[58:61], v201 offset:4544
	v_ldexp_f32 v50, v51, v50
	v_mul_f32_e32 v69, v50, v53
	v_mfma_f32_16x16x32_bf16 v[50:53], v[62:65], v[38:41], v[54:57]
	ds_read_b128 v[62:65], v201 offset:8832
	v_cndmask_b32_e64 v69, 0, v69, s[14:15]
	s_nop 0
	v_mul_f32_e32 v54, v215, v151
	v_cmp_gt_f32_e32 vcc, s53, v54
	s_waitcnt lgkmcnt(1)
	v_mfma_f32_16x16x32_bf16 v[50:53], v[58:61], v[42:45], v[50:53]
	ds_read_b128 v[58:61], v201 offset:8768
	v_cndmask_b32_e32 v54, 0, v210, vcc
	v_fmac_f32_e32 v54, v215, v151
	v_exp_f32_e32 v54, v54
	v_cndmask_b32_e32 v55, 0, v212, vcc
	v_ldexp_f32 v54, v54, v55
	v_mul_f32_e32 v55, v215, v152
	v_cmp_gt_f32_e32 vcc, s53, v55
	v_mul_f32_e32 v50, v54, v50
	v_cndmask_b32_e64 v70, 0, v50, s[16:17]
	v_cndmask_b32_e32 v55, 0, v210, vcc
	v_fmac_f32_e32 v55, v215, v152
	v_exp_f32_e32 v55, v55
	v_cndmask_b32_e32 v50, 0, v212, vcc
	v_ldexp_f32 v50, v55, v50
	v_mul_f32_e32 v50, v50, v51
	v_mul_f32_e32 v51, v215, v153
	ds_read_b128 v[54:57], v201 offset:8704
	v_cmp_gt_f32_e32 vcc, s53, v51
	v_cndmask_b32_e64 v71, 0, v50, s[18:19]
	s_waitcnt lgkmcnt(0)
	v_mfma_f32_16x16x32_bf16 v[54:57], v[54:57], v[22:25], 0
	v_cndmask_b32_e32 v51, 0, v210, vcc
	v_fmac_f32_e32 v51, v215, v153
	v_exp_f32_e32 v51, v51
	v_cndmask_b32_e32 v50, 0, v212, vcc
	v_mfma_f32_16x16x32_bf16 v[54:57], v[58:61], v[46:49], v[54:57]
	ds_read_b128 v[58:61], v201 offset:8896
	v_ldexp_f32 v50, v51, v50
	v_mul_f32_e32 v51, v215, v154
	v_cmp_gt_f32_e32 vcc, s53, v51
	v_mul_f32_e32 v50, v50, v52
	v_cndmask_b32_e64 v72, 0, v50, s[20:21]
	v_cndmask_b32_e32 v51, 0, v210, vcc
	v_fmac_f32_e32 v51, v215, v154
	v_exp_f32_e32 v51, v51
	v_cndmask_b32_e32 v50, 0, v212, vcc
	v_ldexp_f32 v50, v51, v50
	v_mul_f32_e32 v73, v50, v53
	v_mfma_f32_16x16x32_bf16 v[50:53], v[62:65], v[38:41], v[54:57]
	ds_read_b128 v[62:65], v201 offset:13184
	v_cndmask_b32_e64 v73, 0, v73, s[22:23]
	s_nop 0
	v_mul_f32_e32 v54, v215, v155
	v_cmp_gt_f32_e32 vcc, s53, v54
	s_waitcnt lgkmcnt(1)
	v_mfma_f32_16x16x32_bf16 v[50:53], v[58:61], v[42:45], v[50:53]
	ds_read_b128 v[58:61], v201 offset:13120
	v_cndmask_b32_e32 v54, 0, v210, vcc
	v_fmac_f32_e32 v54, v215, v155
	v_exp_f32_e32 v54, v54
	v_cndmask_b32_e32 v55, 0, v212, vcc
	v_ldexp_f32 v54, v54, v55
	v_mul_f32_e32 v55, v215, v156
	v_cmp_gt_f32_e32 vcc, s53, v55
	v_mul_f32_e32 v50, v54, v50
	v_cndmask_b32_e64 v74, 0, v50, s[24:25]
	v_cndmask_b32_e32 v55, 0, v210, vcc
	v_fmac_f32_e32 v55, v215, v156
	v_exp_f32_e32 v55, v55
	v_cndmask_b32_e32 v50, 0, v212, vcc
	v_ldexp_f32 v50, v55, v50
	v_mul_f32_e32 v50, v50, v51
	v_mul_f32_e32 v51, v215, v157
	ds_read_b128 v[54:57], v201 offset:13056
	v_cmp_gt_f32_e32 vcc, s53, v51
	v_cndmask_b32_e64 v75, 0, v50, s[26:27]
	s_waitcnt lgkmcnt(0)
	v_mfma_f32_16x16x32_bf16 v[54:57], v[54:57], v[22:25], 0
	v_cndmask_b32_e32 v51, 0, v210, vcc
	v_fmac_f32_e32 v51, v215, v157
	v_exp_f32_e32 v51, v51
	v_cndmask_b32_e32 v50, 0, v212, vcc
	v_mfma_f32_16x16x32_bf16 v[54:57], v[58:61], v[46:49], v[54:57]
	ds_read_b128 v[58:61], v201 offset:13248
	v_ldexp_f32 v50, v51, v50
	v_mul_f32_e32 v51, v215, v158
	v_cmp_gt_f32_e32 vcc, s53, v51
	v_mul_f32_e32 v50, v50, v52
	v_cndmask_b32_e64 v76, 0, v50, s[28:29]
	v_cndmask_b32_e32 v51, 0, v210, vcc
	v_fmac_f32_e32 v51, v215, v158
	v_exp_f32_e32 v51, v51
	v_cndmask_b32_e32 v50, 0, v212, vcc
	v_ldexp_f32 v50, v51, v50
	v_mul_f32_e32 v77, v50, v53
	v_mfma_f32_16x16x32_bf16 v[50:53], v[62:65], v[38:41], v[54:57]
	ds_read_b128 v[62:65], v201 offset:17536
	v_cndmask_b32_e64 v77, 0, v77, s[30:31]
	s_nop 0
	v_mul_f32_e32 v54, v215, v159
	v_cmp_gt_f32_e32 vcc, s53, v54
	s_waitcnt lgkmcnt(1)
	v_mfma_f32_16x16x32_bf16 v[50:53], v[58:61], v[42:45], v[50:53]
	ds_read_b128 v[58:61], v201 offset:17472
	v_cndmask_b32_e32 v54, 0, v210, vcc
	v_fmac_f32_e32 v54, v215, v159
	v_exp_f32_e32 v54, v54
	v_cndmask_b32_e32 v55, 0, v212, vcc
	v_ldexp_f32 v54, v54, v55
	v_mul_f32_e32 v55, v215, v160
	v_cmp_gt_f32_e32 vcc, s53, v55
	v_mul_f32_e32 v50, v54, v50
	v_cndmask_b32_e64 v78, 0, v50, s[34:35]
	v_cndmask_b32_e32 v55, 0, v210, vcc
	v_fmac_f32_e32 v55, v215, v160
	v_exp_f32_e32 v55, v55
	v_cndmask_b32_e32 v50, 0, v212, vcc
	v_ldexp_f32 v50, v55, v50
	v_mul_f32_e32 v50, v50, v51
	v_mul_f32_e32 v51, v215, v161
	ds_read_b128 v[54:57], v201 offset:17408
	v_cmp_gt_f32_e32 vcc, s53, v51
	v_cndmask_b32_e64 v79, 0, v50, s[36:37]
	s_waitcnt lgkmcnt(0)
	v_mfma_f32_16x16x32_bf16 v[54:57], v[54:57], v[22:25], 0
	v_cndmask_b32_e32 v51, 0, v210, vcc
	v_fmac_f32_e32 v51, v215, v161
	v_exp_f32_e32 v51, v51
	v_cndmask_b32_e32 v50, 0, v212, vcc
	v_mfma_f32_16x16x32_bf16 v[54:57], v[58:61], v[46:49], v[54:57]
	ds_read_b128 v[58:61], v201 offset:17600
	v_ldexp_f32 v50, v51, v50
	v_mul_f32_e32 v51, v215, v162
	v_cmp_gt_f32_e32 vcc, s53, v51
	v_mul_f32_e32 v50, v50, v52
	v_cndmask_b32_e64 v80, 0, v50, s[38:39]
	v_cndmask_b32_e32 v51, 0, v210, vcc
	v_fmac_f32_e32 v51, v215, v162
	v_exp_f32_e32 v51, v51
	v_cndmask_b32_e32 v50, 0, v212, vcc
	v_ldexp_f32 v50, v51, v50
	v_mul_f32_e32 v81, v50, v53
	v_mfma_f32_16x16x32_bf16 v[50:53], v[62:65], v[38:41], v[54:57]
	ds_read_b128 v[62:65], v201 offset:21888
	v_cndmask_b32_e64 v81, 0, v81, s[40:41]
	s_nop 0
	v_mul_f32_e32 v54, v215, v163
	v_cmp_gt_f32_e32 vcc, s53, v54
	s_waitcnt lgkmcnt(1)
	v_mfma_f32_16x16x32_bf16 v[50:53], v[58:61], v[42:45], v[50:53]
	ds_read_b128 v[58:61], v201 offset:21824
	v_cndmask_b32_e32 v54, 0, v210, vcc
	v_fmac_f32_e32 v54, v215, v163
	v_exp_f32_e32 v54, v54
	v_cndmask_b32_e32 v55, 0, v212, vcc
	v_ldexp_f32 v54, v54, v55
	v_mul_f32_e32 v55, v215, v164
	v_cmp_gt_f32_e32 vcc, s53, v55
	v_mul_f32_e32 v50, v54, v50
	v_cndmask_b32_e64 v82, 0, v50, s[42:43]
	v_cndmask_b32_e32 v55, 0, v210, vcc
	v_fmac_f32_e32 v55, v215, v164
	v_exp_f32_e32 v55, v55
	v_cndmask_b32_e32 v50, 0, v212, vcc
	v_ldexp_f32 v50, v55, v50
	v_mul_f32_e32 v50, v50, v51
	v_mul_f32_e32 v51, v215, v165
	ds_read_b128 v[54:57], v201 offset:21760
	v_cmp_gt_f32_e32 vcc, s53, v51
	v_cndmask_b32_e64 v83, 0, v50, s[44:45]
	s_waitcnt lgkmcnt(0)
	v_mfma_f32_16x16x32_bf16 v[54:57], v[54:57], v[22:25], 0
	v_cndmask_b32_e32 v51, 0, v210, vcc
	v_fmac_f32_e32 v51, v215, v165
	v_exp_f32_e32 v51, v51
	v_cndmask_b32_e32 v50, 0, v212, vcc
	v_mfma_f32_16x16x32_bf16 v[54:57], v[58:61], v[46:49], v[54:57]
	ds_read_b128 v[58:61], v201 offset:21952
	v_ldexp_f32 v50, v51, v50
	v_mul_f32_e32 v51, v215, v166
	v_cmp_gt_f32_e32 vcc, s53, v51
	v_mul_f32_e32 v50, v50, v52
	v_cndmask_b32_e64 v84, 0, v50, s[46:47]
	v_cndmask_b32_e32 v51, 0, v210, vcc
	v_fmac_f32_e32 v51, v215, v166
	v_exp_f32_e32 v51, v51
	v_cndmask_b32_e32 v50, 0, v212, vcc
	v_ldexp_f32 v50, v51, v50
	v_mul_f32_e32 v85, v50, v53
	v_mfma_f32_16x16x32_bf16 v[50:53], v[62:65], v[38:41], v[54:57]
	ds_read_b128 v[62:65], v201 offset:26240
	v_cndmask_b32_e64 v85, 0, v85, s[2:3]
	s_nop 0
	v_mul_f32_e32 v54, v215, v168
	v_cmp_gt_f32_e32 vcc, s53, v54
	s_waitcnt lgkmcnt(1)
	v_mfma_f32_16x16x32_bf16 v[50:53], v[58:61], v[42:45], v[50:53]
	ds_read_b128 v[58:61], v201 offset:26176
	v_cndmask_b32_e32 v54, 0, v210, vcc
	v_fmac_f32_e32 v54, v215, v168
	v_exp_f32_e32 v54, v54
	v_cndmask_b32_e32 v55, 0, v212, vcc
	v_ldexp_f32 v54, v54, v55
	v_mul_f32_e32 v55, v215, v169
	v_cmp_gt_f32_e32 vcc, s53, v55
	v_mul_f32_e32 v50, v54, v50
	v_cndmask_b32_e64 v86, 0, v50, s[4:5]
	v_cndmask_b32_e32 v55, 0, v210, vcc
	v_fmac_f32_e32 v55, v215, v169
	v_exp_f32_e32 v55, v55
	v_cndmask_b32_e32 v50, 0, v212, vcc
	v_ldexp_f32 v50, v55, v50
	v_mul_f32_e32 v50, v50, v51
	v_mul_f32_e32 v51, v215, v170
	ds_read_b128 v[54:57], v201 offset:26112
	v_cmp_gt_f32_e32 vcc, s53, v51
	v_cndmask_b32_e64 v87, 0, v50, s[78:79]
	s_waitcnt lgkmcnt(0)
	v_mfma_f32_16x16x32_bf16 v[54:57], v[54:57], v[22:25], 0
	v_cndmask_b32_e32 v51, 0, v210, vcc
	v_fmac_f32_e32 v51, v215, v170
	v_exp_f32_e32 v51, v51
	v_cndmask_b32_e32 v50, 0, v212, vcc
	v_mfma_f32_16x16x32_bf16 v[54:57], v[58:61], v[46:49], v[54:57]
	ds_read_b128 v[58:61], v201 offset:26304
	v_ldexp_f32 v50, v51, v50
	v_mul_f32_e32 v51, v215, v171
	v_cmp_gt_f32_e32 vcc, s53, v51
	v_mul_f32_e32 v50, v50, v52
	v_cndmask_b32_e64 v88, 0, v50, s[54:55]
	v_cndmask_b32_e32 v51, 0, v210, vcc
	v_fmac_f32_e32 v51, v215, v171
	v_exp_f32_e32 v51, v51
	v_cndmask_b32_e32 v50, 0, v212, vcc
	v_ldexp_f32 v50, v51, v50
	v_mul_f32_e32 v89, v50, v53
	v_mfma_f32_16x16x32_bf16 v[50:53], v[62:65], v[38:41], v[54:57]
	v_mul_f32_e32 v62, v215, v175
	v_cndmask_b32_e64 v89, 0, v89, s[56:57]
	s_nop 0
	v_mul_f32_e32 v54, v215, v172
	v_cmp_gt_f32_e32 vcc, s53, v54
	s_waitcnt lgkmcnt(0)
	v_mfma_f32_16x16x32_bf16 v[50:53], v[58:61], v[42:45], v[50:53]
	v_cndmask_b32_e32 v54, 0, v210, vcc
	v_fmac_f32_e32 v54, v215, v172
	v_exp_f32_e32 v54, v54
	v_cndmask_b32_e32 v55, 0, v212, vcc
	v_ldexp_f32 v54, v54, v55
	v_mul_f32_e32 v55, v215, v173
	v_cmp_gt_f32_e32 vcc, s53, v55
	s_nop 0
	v_mul_f32_e32 v50, v54, v50
	v_cndmask_b32_e64 v50, 0, v50, s[58:59]
	v_cndmask_b32_e32 v55, 0, v210, vcc
	v_fmac_f32_e32 v55, v215, v173
	v_exp_f32_e32 v55, v55
	v_cndmask_b32_e32 v54, 0, v212, vcc
	v_ldexp_f32 v54, v55, v54
	v_mul_f32_e32 v51, v54, v51
	v_mul_f32_e32 v54, v215, v174
	v_cmp_gt_f32_e32 vcc, s53, v54
	v_cndmask_b32_e64 v51, 0, v51, s[60:61]
	s_nop 0
	v_cndmask_b32_e32 v54, 0, v210, vcc
	v_fmac_f32_e32 v54, v215, v174
	v_exp_f32_e32 v58, v54
	ds_read_b128 v[54:57], v201 offset:30464
	v_cndmask_b32_e32 v59, 0, v212, vcc
	v_cmp_gt_f32_e32 vcc, s53, v62
	v_ldexp_f32 v58, v58, v59
	v_mul_f32_e32 v52, v58, v52
	ds_read_b128 v[58:61], v201 offset:30528
	ds_read_b128 v[62:65], v201 offset:30592
	s_waitcnt lgkmcnt(2)
	v_mfma_f32_16x16x32_bf16 v[22:25], v[54:57], v[22:25], 0
	v_cndmask_b32_e32 v90, 0, v210, vcc
	v_cndmask_b32_e32 v55, 0, v212, vcc
	v_fmac_f32_e32 v90, v215, v175
	s_waitcnt lgkmcnt(1)
	v_mfma_f32_16x16x32_bf16 v[22:25], v[58:61], v[46:49], v[22:25]
	ds_read_b128 v[46:49], v201 offset:30656
	v_exp_f32_e32 v54, v90
	s_waitcnt lgkmcnt(0)
	v_mfma_f32_16x16x32_bf16 v[22:25], v[62:65], v[38:41], v[22:25]
	v_mul_f32_e32 v38, v215, v176
	v_cmp_gt_f32_e32 vcc, s53, v38
	v_ldexp_f32 v54, v54, v55
	v_mfma_f32_16x16x32_bf16 v[22:25], v[46:49], v[42:45], v[22:25]
	v_cndmask_b32_e32 v38, 0, v210, vcc
	v_fmac_f32_e32 v38, v215, v176
	v_exp_f32_e32 v38, v38
	v_cndmask_b32_e32 v40, 0, v212, vcc
	s_barrier
	v_ldexp_f32 v38, v38, v40
	v_mul_f32_e32 v40, v215, v177
	v_cmp_gt_f32_e32 vcc, s53, v40
	v_mul_f32_e32 v22, v38, v22
	v_cndmask_b32_e64 v38, 0, v22, s[66:67]
	v_cndmask_b32_e32 v40, 0, v210, vcc
	v_fmac_f32_e32 v40, v215, v177
	v_exp_f32_e32 v40, v40
	v_cndmask_b32_e32 v22, 0, v212, vcc
	v_mul_f32_e32 v53, v54, v53
	v_cndmask_b32_e64 v52, 0, v52, s[62:63]
	v_ldexp_f32 v22, v40, v22
	v_mul_f32_e32 v40, v215, v178
	v_cmp_gt_f32_e32 vcc, s53, v40
	v_mul_f32_e32 v22, v22, v23
	v_mul_f32_e32 v23, v215, v179
	v_cndmask_b32_e32 v40, 0, v210, vcc
	v_fmac_f32_e32 v40, v215, v178
	v_exp_f32_e32 v40, v40
	v_cndmask_b32_e64 v41, 0, v22, s[68:69]
	v_cndmask_b32_e32 v22, 0, v212, vcc
	v_cmp_gt_f32_e32 vcc, s53, v23
	v_ldexp_f32 v22, v40, v22
	v_mul_f32_e32 v22, v22, v24
	v_cndmask_b32_e32 v23, 0, v210, vcc
	v_fmac_f32_e32 v23, v215, v179
	v_exp_f32_e32 v23, v23
	v_cndmask_b32_e64 v40, 0, v22, s[70:71]
	v_cndmask_b32_e32 v22, 0, v212, vcc
	v_cvt_pk_bf16_f32 v24, v70, v71
	v_ldexp_f32 v22, v23, v22
	v_mul_f32_e32 v22, v22, v25
	v_cndmask_b32_e64 v42, 0, v22, s[72:73]
	v_cvt_pk_bf16_f32 v22, v66, v67
	v_cvt_pk_bf16_f32 v23, v68, v69
	v_cvt_pk_bf16_f32 v25, v72, v73
	ds_write2_b64 v202, v[22:23], v[24:25] offset1:4
	v_cvt_pk_bf16_f32 v22, v74, v75
	v_cvt_pk_bf16_f32 v23, v76, v77
	v_cvt_pk_bf16_f32 v24, v78, v79
	v_cvt_pk_bf16_f32 v25, v80, v81
	ds_write2_b64 v202, v[22:23], v[24:25] offset0:8 offset1:12
	v_cvt_pk_bf16_f32 v22, v82, v83
	v_cvt_pk_bf16_f32 v23, v84, v85
	v_cvt_pk_bf16_f32 v24, v86, v87
	v_cvt_pk_bf16_f32 v25, v88, v89
	v_cndmask_b32_e64 v39, 0, v53, s[64:65]
	ds_write2_b64 v202, v[22:23], v[24:25] offset0:16 offset1:20
	v_cvt_pk_bf16_f32 v22, v50, v51
	v_cvt_pk_bf16_f32 v23, v52, v39
	v_cvt_pk_bf16_f32 v24, v38, v41
	v_cvt_pk_bf16_f32 v25, v40, v42
	ds_write2_b64 v202, v[22:23], v[24:25] offset0:24 offset1:28
	s_waitcnt lgkmcnt(0)
	s_barrier
	ds_read_b128 v[22:25], v203
	ds_read_b128 v[38:41], v203 offset:64
	ds_read_b128 v[46:49], v203 offset:4352
	ds_read_b128 v[50:53], v203 offset:4416
	ds_read_b128 v[58:61], v203 offset:8704
	ds_read_b128 v[62:65], v203 offset:8768
	ds_read_b128 v[70:73], v203 offset:13056
	ds_read_b128 v[74:77], v203 offset:13120
	ds_read_b128 v[82:85], v203 offset:17408
	ds_read_b128 v[86:89], v203 offset:17472
	ds_read_b128 v[94:97], v203 offset:21760
	ds_read_b128 v[98:101], v203 offset:21824
	ds_read_b128 v[106:109], v203 offset:26112
	ds_read_b128 v[110:113], v203 offset:26176
	ds_read_b128 v[118:121], v203 offset:30464
	ds_read_b128 v[216:219], v203 offset:30528
	s_waitcnt vmcnt(7) lgkmcnt(14)
	v_mfma_f32_16x16x32_bf16 v[42:45], v[30:33], v[22:25], 0
	s_waitcnt vmcnt(3)
	v_mfma_f32_16x16x32_bf16 v[22:25], v[34:37], v[22:25], 0
	s_waitcnt lgkmcnt(13)
	v_mfma_f32_16x16x32_bf16 v[54:57], v[30:33], v[46:49], 0
	v_mfma_f32_16x16x32_bf16 v[46:49], v[34:37], v[46:49], 0
	s_waitcnt lgkmcnt(11)
	v_mfma_f32_16x16x32_bf16 v[66:69], v[30:33], v[58:61], 0
	v_mfma_f32_16x16x32_bf16 v[58:61], v[34:37], v[58:61], 0
	s_waitcnt lgkmcnt(9)
	v_mfma_f32_16x16x32_bf16 v[78:81], v[30:33], v[70:73], 0
	v_mfma_f32_16x16x32_bf16 v[70:73], v[34:37], v[70:73], 0
	s_waitcnt lgkmcnt(7)
	v_mfma_f32_16x16x32_bf16 v[90:93], v[30:33], v[82:85], 0
	v_mfma_f32_16x16x32_bf16 v[82:85], v[34:37], v[82:85], 0
	s_waitcnt lgkmcnt(5)
	v_mfma_f32_16x16x32_bf16 v[102:105], v[30:33], v[94:97], 0
	v_mfma_f32_16x16x32_bf16 v[94:97], v[34:37], v[94:97], 0
	s_waitcnt lgkmcnt(3)
	v_mfma_f32_16x16x32_bf16 v[114:117], v[30:33], v[106:109], 0
	v_mfma_f32_16x16x32_bf16 v[106:109], v[34:37], v[106:109], 0
	s_waitcnt lgkmcnt(1)
	v_mfma_f32_16x16x32_bf16 v[30:33], v[30:33], v[118:121], 0
	v_mfma_f32_16x16x32_bf16 v[34:37], v[34:37], v[118:121], 0
	v_mfma_f32_16x16x32_bf16 v[42:45], v[18:21], v[38:41], v[42:45]
	s_waitcnt vmcnt(2)
	v_mfma_f32_16x16x32_bf16 v[22:25], v[26:29], v[38:41], v[22:25]
	v_mfma_f32_16x16x32_bf16 v[38:41], v[18:21], v[50:53], v[54:57]
	v_mfma_f32_16x16x32_bf16 v[46:49], v[26:29], v[50:53], v[46:49]
	v_mfma_f32_16x16x32_bf16 v[50:53], v[18:21], v[62:65], v[66:69]
	v_mfma_f32_16x16x32_bf16 v[54:57], v[26:29], v[62:65], v[58:61]
	v_mfma_f32_16x16x32_bf16 v[58:61], v[18:21], v[74:77], v[78:81]
	v_mfma_f32_16x16x32_bf16 v[62:65], v[26:29], v[74:77], v[70:73]
	v_mfma_f32_16x16x32_bf16 v[66:69], v[18:21], v[86:89], v[90:93]
	v_mfma_f32_16x16x32_bf16 v[70:73], v[26:29], v[86:89], v[82:85]
	v_mfma_f32_16x16x32_bf16 v[74:77], v[18:21], v[98:101], v[102:105]
	v_mfma_f32_16x16x32_bf16 v[78:81], v[26:29], v[98:101], v[94:97]
	v_mfma_f32_16x16x32_bf16 v[82:85], v[18:21], v[110:113], v[114:117]
	v_mfma_f32_16x16x32_bf16 v[86:89], v[26:29], v[110:113], v[106:109]
	s_waitcnt lgkmcnt(0)
	v_mfma_f32_16x16x32_bf16 v[18:21], v[18:21], v[216:219], v[30:33]
	v_mfma_f32_16x16x32_bf16 v[26:29], v[26:29], v[216:219], v[34:37]
	s_nop 1
	ds_read_b128 v[30:33], v203 offset:128
	ds_read_b128 v[34:37], v203 offset:192
	s_waitcnt lgkmcnt(1)
	v_mfma_f32_16x16x32_bf16 v[42:45], v[10:13], v[30:33], v[42:45]
	s_waitcnt vmcnt(1)
	v_mfma_f32_16x16x32_bf16 v[22:25], v[14:17], v[30:33], v[22:25]
	ds_read_b128 v[30:33], v203 offset:4480
	ds_read_b128 v[90:93], v203 offset:4544
	s_waitcnt lgkmcnt(1)
	v_mfma_f32_16x16x32_bf16 v[38:41], v[10:13], v[30:33], v[38:41]
	v_mfma_f32_16x16x32_bf16 v[30:33], v[14:17], v[30:33], v[46:49]
	s_nop 2
	ds_read_b128 v[46:49], v203 offset:8832
	ds_read_b128 v[94:97], v203 offset:8896
	s_waitcnt lgkmcnt(1)
	v_mfma_f32_16x16x32_bf16 v[50:53], v[10:13], v[46:49], v[50:53]
	v_mfma_f32_16x16x32_bf16 v[46:49], v[14:17], v[46:49], v[54:57]
	s_nop 2
	ds_read_b128 v[54:57], v203 offset:13184
	ds_read_b128 v[98:101], v203 offset:13248
	s_waitcnt lgkmcnt(1)
	v_mfma_f32_16x16x32_bf16 v[58:61], v[10:13], v[54:57], v[58:61]
	v_mfma_f32_16x16x32_bf16 v[54:57], v[14:17], v[54:57], v[62:65]
	s_nop 2
	ds_read_b128 v[62:65], v203 offset:17536
	ds_read_b128 v[102:105], v203 offset:17600
	s_waitcnt lgkmcnt(1)
	v_mfma_f32_16x16x32_bf16 v[66:69], v[10:13], v[62:65], v[66:69]
	v_mfma_f32_16x16x32_bf16 v[62:65], v[14:17], v[62:65], v[70:73]
	s_nop 2
	ds_read_b128 v[70:73], v203 offset:21888
	ds_read_b128 v[106:109], v203 offset:21952
	s_waitcnt lgkmcnt(1)
	v_mfma_f32_16x16x32_bf16 v[74:77], v[10:13], v[70:73], v[74:77]
	v_mfma_f32_16x16x32_bf16 v[70:73], v[14:17], v[70:73], v[78:81]
	s_nop 2
	ds_read_b128 v[78:81], v203 offset:26240
	ds_read_b128 v[110:113], v203 offset:26304
	s_waitcnt lgkmcnt(1)
	v_mfma_f32_16x16x32_bf16 v[82:85], v[10:13], v[78:81], v[82:85]
	v_mfma_f32_16x16x32_bf16 v[78:81], v[14:17], v[78:81], v[86:89]
	s_nop 2
	ds_read_b128 v[86:89], v203 offset:30592
	ds_read_b128 v[114:117], v203 offset:30656
	s_waitcnt lgkmcnt(1)
	v_mfma_f32_16x16x32_bf16 v[10:13], v[10:13], v[86:89], v[18:21]
	v_mfma_f32_16x16x32_bf16 v[14:17], v[14:17], v[86:89], v[26:29]
	v_mfma_f32_16x16x32_bf16 v[18:21], v[2:5], v[34:37], v[42:45]
	v_mfma_f32_16x16x32_bf16 v[26:29], v[2:5], v[90:93], v[38:41]
	v_mfma_f32_16x16x32_bf16 v[38:41], v[2:5], v[94:97], v[50:53]
	v_mfma_f32_16x16x32_bf16 v[50:53], v[2:5], v[98:101], v[58:61]
	v_mfma_f32_16x16x32_bf16 v[66:69], v[2:5], v[102:105], v[66:69]
	v_mfma_f32_16x16x32_bf16 v[74:77], v[2:5], v[106:109], v[74:77]
	v_mfma_f32_16x16x32_bf16 v[82:85], v[2:5], v[110:113], v[82:85]
	s_waitcnt lgkmcnt(0)
	v_mfma_f32_16x16x32_bf16 v[2:5], v[2:5], v[114:117], v[10:13]
	ds_read_b64_tr_b16 v[10:11], v180 offset:0
	ds_read_b64_tr_b16 v[12:13], v180 offset:0x840
	ds_read_b64_tr_b16 v[86:87], v180 offset:32
	ds_read_b64_tr_b16 v[88:89], v180 offset:0x860
	s_waitcnt vmcnt(0)
	v_mfma_f32_16x16x32_bf16 v[22:25], v[6:9], v[34:37], v[22:25]
	s_waitcnt lgkmcnt(0)
	v_mfma_f32_16x16x32_bf16 v[34:37], v[6:9], v[90:93], v[30:33]
	v_mfma_f32_16x16x32_bf16 v[46:49], v[6:9], v[94:97], v[46:49]
	v_mfma_f32_16x16x32_bf16 v[54:57], v[6:9], v[98:101], v[54:57]
	v_mfma_f32_16x16x32_bf16 v[62:65], v[6:9], v[102:105], v[62:65]
	v_mfma_f32_16x16x32_bf16 v[70:73], v[6:9], v[106:109], v[70:73]
	v_mfma_f32_16x16x32_bf16 v[78:81], v[6:9], v[110:113], v[78:81]
	v_mfma_f32_16x16x32_bf16 v[6:9], v[6:9], v[114:117], v[14:17]
	s_nop 2
	ds_read_b128 v[14:17], v204
	ds_read_b128 v[90:93], v204 offset:4352
	s_waitcnt lgkmcnt(1)
	v_mfma_f32_16x16x32_bf16 v[58:61], v[10:13], v[14:17], v[18:21]
	v_mfma_f32_16x16x32_bf16 v[42:45], v[86:89], v[14:17], v[22:25]
	s_nop 1
	ds_read_b128 v[18:21], v204 offset:8704
	ds_read_b128 v[22:25], v204 offset:13056
	s_waitcnt lgkmcnt(2)
	v_mfma_f32_16x16x32_bf16 v[30:33], v[10:13], v[90:93], v[26:29]
	s_waitcnt lgkmcnt(1)
	v_mfma_f32_16x16x32_bf16 v[26:29], v[10:13], v[18:21], v[38:41]
	v_mfma_f32_16x16x32_bf16 v[18:21], v[86:89], v[18:21], v[46:49]
	s_nop 1
	ds_read_b128 v[38:41], v204 offset:17408
	ds_read_b128 v[46:49], v204 offset:21760
	v_mfma_f32_16x16x32_bf16 v[14:17], v[86:89], v[90:93], v[34:37]
	s_waitcnt lgkmcnt(2)
	v_mfma_f32_16x16x32_bf16 v[34:37], v[10:13], v[22:25], v[50:53]
	v_mfma_f32_16x16x32_bf16 v[22:25], v[86:89], v[22:25], v[54:57]
	s_waitcnt lgkmcnt(1)
	v_mfma_f32_16x16x32_bf16 v[50:53], v[10:13], v[38:41], v[66:69]
	v_mfma_f32_16x16x32_bf16 v[38:41], v[86:89], v[38:41], v[62:65]
	s_waitcnt lgkmcnt(0)
	v_mfma_f32_16x16x32_bf16 v[54:57], v[10:13], v[46:49], v[74:77]
	v_mfma_f32_16x16x32_bf16 v[66:69], v[86:89], v[46:49], v[70:73]
	ds_read_b128 v[46:49], v204 offset:26112
	ds_read_b128 v[62:65], v204 offset:30464
	s_waitcnt lgkmcnt(1)
	v_mfma_f32_16x16x32_bf16 v[70:73], v[10:13], v[46:49], v[82:85]
	s_waitcnt lgkmcnt(0)
	v_mfma_f32_16x16x32_bf16 v[2:5], v[10:13], v[62:65], v[2:5]
	ds_read_b64_tr_b16 v[10:11], v180 offset:0x4200
	ds_read_b64_tr_b16 v[12:13], v180 offset:0x4a40
	v_mfma_f32_16x16x32_bf16 v[74:77], v[86:89], v[46:49], v[78:81]
	ds_read_b64_tr_b16 v[78:79], v180 offset:0x4220
	ds_read_b64_tr_b16 v[80:81], v180 offset:0x4a60
	s_nop 0
	s_waitcnt lgkmcnt(0)
	ds_read_b128 v[46:49], v204 offset:8768
	ds_read_b128 v[82:85], v204 offset:13120
	v_mfma_f32_16x16x32_bf16 v[6:9], v[86:89], v[62:65], v[6:9]
	s_waitcnt lgkmcnt(1)
	v_mfma_f32_16x16x32_bf16 v[62:65], v[10:13], v[46:49], v[26:29]
	v_mfma_f32_16x16x32_bf16 v[46:49], v[78:81], v[46:49], v[18:21]
	s_waitcnt lgkmcnt(0)
	v_mfma_f32_16x16x32_bf16 v[18:21], v[78:81], v[82:85], v[22:25]
	s_nop 2
	ds_read_b128 v[22:25], v204 offset:17472
	ds_read_b128 v[26:29], v204 offset:21824
	v_mfma_f32_16x16x32_bf16 v[34:37], v[10:13], v[82:85], v[34:37]
	s_waitcnt lgkmcnt(1)
	v_mfma_f32_16x16x32_bf16 v[50:53], v[10:13], v[22:25], v[50:53]
	v_mfma_f32_16x16x32_bf16 v[22:25], v[78:81], v[22:25], v[38:41]
	s_waitcnt lgkmcnt(0)
	v_mfma_f32_16x16x32_bf16 v[82:85], v[10:13], v[26:29], v[54:57]
	s_nop 0
	ds_read_b128 v[38:41], v204 offset:26176
	s_nop 0
	ds_read_b128 v[54:57], v204 offset:30528
	v_mfma_f32_16x16x32_bf16 v[26:29], v[78:81], v[26:29], v[66:69]
	s_waitcnt lgkmcnt(1)
	v_mfma_f32_16x16x32_bf16 v[66:69], v[10:13], v[38:41], v[70:73]
	v_mfma_f32_16x16x32_bf16 v[70:73], v[78:81], v[38:41], v[74:77]
	ds_read_b64_tr_b16 v[74:75], v180 offset:0x8400
	ds_read_b64_tr_b16 v[76:77], v180 offset:0x8c40
	s_waitcnt lgkmcnt(0)
	v_mfma_f32_16x16x32_bf16 v[2:5], v[10:13], v[54:57], v[2:5]
	v_mfma_f32_16x16x32_bf16 v[10:13], v[78:81], v[54:57], v[6:9]
	ds_read_b64_tr_b16 v[78:79], v180 offset:0x8420
	ds_read_b64_tr_b16 v[80:81], v180 offset:0x8c60
	s_nop 0
	s_waitcnt lgkmcnt(0)
	s_nop 1
	ds_read_b128 v[6:9], v204 offset:17536
	ds_read_b128 v[86:89], v204 offset:21888
	s_waitcnt lgkmcnt(1)
	v_mfma_f32_16x16x32_bf16 v[54:57], v[74:77], v[6:9], v[50:53]
	v_mfma_f32_16x16x32_bf16 v[38:41], v[78:81], v[6:9], v[22:25]
	s_waitcnt lgkmcnt(0)
	v_mfma_f32_16x16x32_bf16 v[6:9], v[78:81], v[86:89], v[26:29]
	s_nop 2
	ds_read_b128 v[26:29], v204 offset:26240
	ds_read_b128 v[50:53], v204 offset:30592
	v_mfma_f32_16x16x32_bf16 v[22:25], v[74:77], v[86:89], v[82:85]
	s_waitcnt lgkmcnt(1)
	v_mfma_f32_16x16x32_bf16 v[66:69], v[74:77], v[26:29], v[66:69]
	s_waitcnt lgkmcnt(0)
	v_mfma_f32_16x16x32_bf16 v[2:5], v[74:77], v[50:53], v[2:5]
	ds_read_b64_tr_b16 v[74:75], v180 offset:0xc600
	ds_read_b64_tr_b16 v[76:77], v180 offset:0xce40
	v_mfma_f32_16x16x32_bf16 v[70:73], v[78:81], v[26:29], v[70:73]
	v_mfma_f32_16x16x32_bf16 v[50:53], v[78:81], v[50:53], v[10:13]
	ds_read_b64_tr_b16 v[78:79], v180 offset:0xc620
	ds_read_b64_tr_b16 v[80:81], v180 offset:0xce60
	s_nop 0
	s_waitcnt lgkmcnt(0)
	s_nop 1
	ds_read_b128 v[10:13], v204 offset:26304
	ds_read_b128 v[82:85], v204 offset:30656
	s_waitcnt lgkmcnt(1)
	v_mfma_f32_16x16x32_bf16 v[26:29], v[74:77], v[10:13], v[66:69]
	s_nop 2
	v_and_b32_e32 v67, 64, v213
	v_xor_b32_e32 v66, 16, v213
	v_pk_mul_f32 v[68:69], v[58:59], v[58:59]
	v_mfma_f32_16x16x32_bf16 v[10:13], v[78:81], v[10:13], v[70:73]
	v_fmac_f32_e32 v69, v58, v58
	s_nop 1
	v_add_u32_e32 v71, 64, v67
	v_cmp_lt_i32_e32 vcc, v66, v71
	s_waitcnt lgkmcnt(0)
	v_mfma_f32_16x16x32_bf16 v[2:5], v[74:77], v[82:85], v[2:5]
	v_cndmask_b32_e32 v66, v213, v66, vcc
	v_lshlrev_b32_e32 v70, 2, v66
	v_add_f32_e32 v66, 0, v58
	v_add_f32_e32 v66, v59, v66
	v_add_f32_e32 v72, v60, v66
	v_pk_mul_f32 v[66:67], v[60:61], v[60:61]
	v_mfma_f32_16x16x32_bf16 v[50:53], v[78:81], v[82:85], v[50:53]
	v_add_f32_e32 v68, v66, v69
	v_add_f32_e32 v66, v61, v72
	v_add_f32_e32 v69, v42, v66
	v_mov_b32_e32 v66, v42
	v_mov_b32_e32 v67, v61
	v_pk_mul_f32 v[66:67], v[66:67], v[66:67]
	v_pk_mul_f32 v[72:73], v[42:43], v[42:43]
	v_add_f32_e32 v67, v67, v68
	v_add_f32_e32 v67, v66, v67
	v_add_f32_e32 v66, v43, v69
	v_pk_mul_f32 v[68:69], v[44:45], v[44:45]
	v_add_f32_e32 v67, v73, v67
	v_add_f32_e32 v66, v44, v66
	v_add_f32_e32 v69, v68, v67
	v_mul_f32_e32 v67, v45, v45
	v_mov_b32_e32 v68, v45
	v_pk_add_f32 v[66:67], v[68:69], v[66:67]
	ds_bpermute_b32 v68, v70, v66
	ds_bpermute_b32 v69, v70, v67
	v_xor_b32_e32 v72, 32, v213
	v_cmp_lt_i32_e32 vcc, v72, v71
	s_waitcnt lgkmcnt(0)
	v_pk_add_f32 v[66:67], v[66:67], v[68:69]
	v_cndmask_b32_e32 v71, v213, v72, vcc
	v_lshlrev_b32_e32 v71, 2, v71
	ds_bpermute_b32 v68, v71, v66
	ds_bpermute_b32 v69, v71, v67
	s_and_saveexec_b64 s[0:1], s[74:75]
	s_cbranch_execz .LBB0_940
	v_readlane_b32 s94, v254, 20
	s_waitcnt lgkmcnt(0)
	v_pk_add_f32 v[66:67], v[66:67], v[68:69]
	v_add_u32_e32 v68, s94, v181
	ds_write_b64 v68, v[66:67]
